# speedup vs baseline: 1.0413x; 1.0413x over previous
_Z17prep_count_kernelPKfS0_S0_S0_S0_S0_S0_PDF16_PjPfS1_PKiS5_Pi:
	s_cmp_gt_u32 s2, 8
	s_mov_b64 s[4:5], -1
	s_cbranch_scc0 .LBB0_16
	s_load_dwordx4 s[8:11], s[0:1], 0x58
	s_movk_i32 s3, 0x100
	v_cmp_gt_u32_e64 s[4:5], s3, v0
	v_lshlrev_b32_e32 v2, 2, v0
	s_and_saveexec_b64 s[6:7], s[4:5]
	v_mov_b32_e32 v1, 0
	ds_write_b32 v2, v1
	s_or_b64 exec, exec, s[6:7]
	s_add_i32 s3, s2, -9
	s_ashr_i32 s6, s3, 31
	s_lshr_b32 s6, s6, 25
	s_add_i32 s12, s3, s6
	s_and_b32 s6, s12, 0xffffff80
	s_sub_i32 s3, s3, s6
	s_add_i32 s6, s2, 0x76
	s_cmpk_lt_u32 s6, 0xff
	s_mul_i32 s6, s3, 0x186a
	s_waitcnt lgkmcnt(0)
	s_cselect_b32 s9, s9, s11
	s_cselect_b32 s8, s8, s10
	s_ashr_i32 s7, s6, 31
	s_lshl_b64 s[6:7], s[6:7], 2
	s_add_u32 s6, s8, s6
	s_addc_u32 s7, s9, s7
	v_mov_b32_e32 v3, 0
	v_lshl_add_u64 v[4:5], s[6:7], 0, v[2:3]
	s_movk_i32 s8, 0x2000
	v_add_co_u32_e32 v10, vcc, s8, v4
	s_movk_i32 s8, 0x4000
	s_nop 0
	v_addc_co_u32_e32 v11, vcc, 0, v5, vcc
	v_add_co_u32_e32 v12, vcc, s8, v4
	s_movk_i32 s8, 0x186a
	s_nop 0
	v_addc_co_u32_e32 v13, vcc, 0, v5, vcc
	v_add_co_u32_e32 v14, vcc, 0x5000, v4
	v_or_b32_e32 v9, 0x1800, v0
	s_nop 0
	v_addc_co_u32_e32 v15, vcc, 0, v5, vcc
	global_load_dword v8, v2, s[6:7] nt
	global_load_dword v7, v[10:11], off offset:-4096 nt
	global_load_dword v6, v[10:11], off nt
	global_load_dword v5, v[12:13], off offset:-4096 nt
	global_load_dword v4, v[12:13], off nt
	global_load_dword v3, v[14:15], off nt
	v_cmp_gt_u32_e32 vcc, s8, v9
	v_mov_b32_e32 v1, -1
	s_and_saveexec_b64 s[8:9], vcc
	s_cbranch_execz .LBB0_5
	v_lshlrev_b32_e32 v1, 2, v9
	global_load_dword v1, v1, s[6:7] nt

.LBB1_2:
	s_or_b64 exec, exec, s[6:7]
	s_mul_i32 s12, s2, 0xc35
	v_lshrrev_b32_e32 v155, 5, v0
	s_ashr_i32 s6, s12, 4
	v_and_or_b32 v11, s6, -16, v155
	v_min_i32_e32 v2, 0xc34f, v11
	v_and_b32_e32 v146, 0x1f0, v10
	v_ashrrev_i32_e32 v3, 31, v2
	s_waitcnt lgkmcnt(0)
	v_lshl_add_u64 v[12:13], s[24:25], 0, v[146:147]
	v_lshlrev_b64 v[2:3], 9, v[2:3]
	v_lshl_add_u64 v[14:15], v[12:13], 0, v[2:3]
	v_min_i32_e32 v2, 0xc33f, v11
	v_ashrrev_i32_e32 v3, 31, v2
	v_lshlrev_b64 v[2:3], 9, v[2:3]
	v_lshl_add_u64 v[2:3], v[12:13], 0, v[2:3]
	s_movk_i32 s6, 0x2000
	v_add_co_u32_e32 v16, vcc, s6, v2
	s_movk_i32 s7, 0x4000
	s_nop 0
	v_addc_co_u32_e32 v17, vcc, 0, v3, vcc
	global_load_dwordx4 v[2:5], v[14:15], off nt
	global_load_dwordx4 v[6:9], v[16:17], off nt
	v_min_i32_e32 v14, 0xc32f, v11
	v_ashrrev_i32_e32 v15, 31, v14
	v_lshlrev_b64 v[14:15], 9, v[14:15]
	v_min_i32_e32 v16, 0xc31f, v11
	v_lshl_add_u64 v[14:15], v[12:13], 0, v[14:15]
	v_ashrrev_i32_e32 v17, 31, v16
	v_lshrrev_b32_e32 v1, 6, v0
	v_add_co_u32_e32 v14, vcc, s7, v14
	v_lshlrev_b64 v[16:17], 9, v[16:17]
	s_nop 0
	v_addc_co_u32_e32 v15, vcc, 0, v15, vcc
	v_lshl_add_u64 v[12:13], v[12:13], 0, v[16:17]
	s_movk_i32 s7, 0x6000
	v_and_b32_e32 v146, 0x3f0, v10
	v_mul_u32_u24_e32 v10, 0x1800, v1
	v_add_co_u32_e32 v12, vcc, s7, v12
	v_lshl_add_u64 v[54:55], s[26:27], 0, v[146:147]
	v_lshlrev_b32_e32 v146, 1, v10
	v_addc_co_u32_e32 v13, vcc, 0, v13, vcc
	v_lshl_add_u64 v[26:27], v[54:55], 0, v[146:147]
	s_movk_i32 s7, 0x1000
	v_add_co_u32_e32 v56, vcc, s7, v26
	global_load_dwordx4 v[74:77], v[14:15], off nt
	global_load_dwordx4 v[78:81], v[12:13], off nt
	v_addc_co_u32_e32 v57, vcc, 0, v27, vcc
	v_add_co_u32_e32 v50, vcc, s6, v26
	s_mov_b32 s6, 0x18000
	s_nop 0
	v_addc_co_u32_e32 v51, vcc, 0, v27, vcc
	global_load_dwordx4 v[10:13], v[26:27], off
	global_load_dwordx4 v[14:17], v[26:27], off offset:1024
	global_load_dwordx4 v[18:21], v[26:27], off offset:2048
	global_load_dwordx4 v[22:25], v[26:27], off offset:3072
	s_nop 0
	global_load_dwordx4 v[26:29], v[56:57], off offset:1024
	global_load_dwordx4 v[30:33], v[56:57], off offset:2048
	global_load_dwordx4 v[34:37], v[50:51], off offset:-4096
	global_load_dwordx4 v[38:41], v[50:51], off
	global_load_dwordx4 v[42:45], v[50:51], off offset:1024
	global_load_dwordx4 v[46:49], v[50:51], off offset:2048
	s_nop 0
	global_load_dwordx4 v[50:53], v[50:51], off offset:3072
	v_add_co_u32_e32 v70, vcc, s6, v54
	v_and_b32_e32 v146, 15, v0
	s_nop 0
	v_addc_co_u32_e32 v71, vcc, 0, v55, vcc
	v_mul_u32_u24_e32 v148, 48, v1
	s_movk_i32 s6, 0x70
	v_mad_u32_u24 v151, v1, 48, 32
	global_load_dwordx4 v[54:57], v[56:57], off offset:3072
	s_nop 0
	global_load_dwordx4 v[58:61], v[70:71], off
	global_load_dwordx4 v[62:65], v[70:71], off offset:1024
	global_load_dwordx4 v[66:69], v[70:71], off offset:2048
	s_nop 0
	global_load_dwordx4 v[70:73], v[70:71], off offset:3072
	v_and_or_b32 v148, v148, s6, v146
	v_mad_u32_u24 v149, v1, 48, 16
	v_and_or_b32 v151, v151, s6, v146
	v_lshlrev_b32_e32 v148, 2, v148
	v_and_or_b32 v149, v149, s6, v146
	v_lshlrev_b32_e32 v152, 2, v151
	v_lshlrev_b32_e32 v149, 2, v149
	global_load_dword v153, v148, s[4:5]
	global_load_dword v151, v149, s[4:5]
	s_nop 0
	global_load_dword v152, v152, s[4:5]
	v_mbcnt_lo_u32_b32 v148, -1, 0
	v_mov_b32_e32 v164, 0
	v_mov_b32_e32 v163, 0
	v_mov_b32_e32 v162, 0
	v_mov_b32_e32 v149, 0
	s_and_saveexec_b64 s[6:7], s[8:9]
	s_cbranch_execz .LBB1_6
	s_and_b32 s10, s3, 7
	s_cmp_lg_u32 s10, 0
	s_cselect_b64 s[4:5], -1, 0
	s_cmp_gt_u32 s10, 1
	v_cndmask_b32_e64 v149, 0, 1, s[4:5]
	s_cselect_b32 s4, 0x10000, 0
	s_cmp_gt_u32 s10, 2
	v_or_b32_e32 v149, s4, v149
	s_cselect_b64 s[4:5], -1, 0
	v_cndmask_b32_e64 v154, 0, 1, s[4:5]
	s_lshl_b32 s4, s3, 14
	s_and_b32 s4, s4, 0x10000
	s_cmp_gt_u32 s10, 4
	v_or_b32_e32 v154, s4, v154
	s_cselect_b64 s[4:5], -1, 0
	s_cmp_gt_u32 s10, 5
	v_cndmask_b32_e64 v156, 0, 1, s[4:5]
	s_cselect_b32 s4, 0x10000, 0
	s_cmp_eq_u32 s10, 7
	v_or_b32_e32 v156, s4, v156
	s_cselect_b64 s[4:5], -1, 0
	v_cndmask_b32_e64 v157, 0, 1, s[4:5]
	s_mov_b32 s5, 0x10001
	v_dot2_u32_u16 v158, v142, s5, 0
	s_ashr_i32 s4, s3, 3
	v_dot2_u32_u16 v158, v143, s5, v158
	s_cmp_gt_i32 s4, 0
	v_dot2_u32_u16 v158, v144, s5, v158
	s_cselect_b64 vcc, -1, 0
	v_dot2_u32_u16 v158, v145, s5, v158
	s_cmp_lt_u32 s3, 8
	v_and_b32_e32 v147, 63, v0
	s_nop 0
	v_cndmask_b32_e32 v159, 0, v158, vcc
	v_dot2_u32_u16 v142, v142, v149, v159
	s_cselect_b64 vcc, -1, 0
	v_dot2_u32_u16 v142, v143, v154, v142
	v_dot2_u32_u16 v143, v138, s5, 0
	v_dot2_u32_u16 v142, v144, v156, v142
	v_dot2_u32_u16 v143, v139, s5, v143
	v_dot2_u32_u16 v142, v145, v157, v142
	v_dot2_u32_u16 v143, v140, s5, v143
	s_cmp_gt_i32 s4, 1
	v_dot2_u32_u16 v143, v141, s5, v143
	v_cndmask_b32_e32 v142, v159, v142, vcc
	s_cselect_b64 vcc, -1, 0
	s_cmp_eq_u32 s4, 1
	v_add_u32_e32 v144, v143, v158
	v_cndmask_b32_e32 v143, 0, v143, vcc
	v_add_u32_e32 v142, v143, v142
	v_dot2_u32_u16 v138, v138, v149, v142
	s_cselect_b64 vcc, -1, 0
	v_dot2_u32_u16 v138, v139, v154, v138
	v_dot2_u32_u16 v139, v134, s5, 0
	v_dot2_u32_u16 v138, v140, v156, v138
	v_dot2_u32_u16 v139, v135, s5, v139
	v_dot2_u32_u16 v138, v141, v157, v138
	v_dot2_u32_u16 v139, v136, s5, v139
	s_cmp_gt_i32 s4, 2
	v_dot2_u32_u16 v139, v137, s5, v139
	v_cndmask_b32_e32 v138, v142, v138, vcc
	s_cselect_b64 vcc, -1, 0
	s_cmp_eq_u32 s4, 2
	v_cndmask_b32_e32 v140, 0, v139, vcc
	v_add_u32_e32 v138, v140, v138
	v_dot2_u32_u16 v134, v134, v149, v138
	s_cselect_b64 vcc, -1, 0
	v_dot2_u32_u16 v134, v135, v154, v134
	v_dot2_u32_u16 v135, v130, s5, 0
	v_dot2_u32_u16 v134, v136, v156, v134
	v_dot2_u32_u16 v135, v131, s5, v135
	v_dot2_u32_u16 v134, v137, v157, v134
	v_dot2_u32_u16 v135, v132, s5, v135
	s_cmp_gt_i32 s4, 3
	v_dot2_u32_u16 v135, v133, s5, v135
	v_cndmask_b32_e32 v134, v138, v134, vcc
	s_cselect_b64 vcc, -1, 0
	s_cmp_eq_u32 s4, 3
	v_add3_u32 v136, v139, v144, v135
	v_cndmask_b32_e32 v135, 0, v135, vcc
	v_add_u32_e32 v134, v135, v134
	v_dot2_u32_u16 v130, v130, v149, v134
	s_cselect_b64 vcc, -1, 0
	v_dot2_u32_u16 v130, v131, v154, v130
	v_dot2_u32_u16 v131, v126, s5, 0
	v_dot2_u32_u16 v130, v132, v156, v130
	v_dot2_u32_u16 v131, v127, s5, v131
	v_dot2_u32_u16 v130, v133, v157, v130
	v_dot2_u32_u16 v131, v128, s5, v131
	s_cmp_gt_i32 s4, 4
	v_dot2_u32_u16 v131, v129, s5, v131
	v_cndmask_b32_e32 v130, v134, v130, vcc
	s_cselect_b64 vcc, -1, 0
	s_cmp_eq_u32 s4, 4
	v_cndmask_b32_e32 v132, 0, v131, vcc
	v_add_u32_e32 v130, v132, v130
	v_dot2_u32_u16 v126, v126, v149, v130
	s_cselect_b64 vcc, -1, 0
	v_dot2_u32_u16 v126, v127, v154, v126
	v_dot2_u32_u16 v127, v122, s5, 0
	v_dot2_u32_u16 v126, v128, v156, v126
	v_dot2_u32_u16 v127, v123, s5, v127
	v_dot2_u32_u16 v126, v129, v157, v126
	v_dot2_u32_u16 v127, v124, s5, v127
	s_cmp_gt_i32 s4, 5
	v_dot2_u32_u16 v127, v125, s5, v127
	v_cndmask_b32_e32 v126, v130, v126, vcc
	s_cselect_b64 vcc, -1, 0
	s_cmp_eq_u32 s4, 5
	v_add3_u32 v128, v131, v136, v127
	v_cndmask_b32_e32 v127, 0, v127, vcc
	v_add_u32_e32 v126, v127, v126
	v_dot2_u32_u16 v122, v122, v149, v126
	s_cselect_b64 vcc, -1, 0
	v_dot2_u32_u16 v122, v123, v154, v122
	v_dot2_u32_u16 v123, v118, s5, 0
	v_dot2_u32_u16 v122, v124, v156, v122
	v_dot2_u32_u16 v123, v119, s5, v123
	v_dot2_u32_u16 v122, v125, v157, v122
	v_dot2_u32_u16 v123, v120, s5, v123
	s_cmp_gt_i32 s4, 6
	v_dot2_u32_u16 v123, v121, s5, v123
	v_cndmask_b32_e32 v122, v126, v122, vcc
	s_cselect_b64 vcc, -1, 0
	s_cmp_eq_u32 s4, 6
	v_cndmask_b32_e32 v124, 0, v123, vcc
	v_add_u32_e32 v122, v124, v122
	v_dot2_u32_u16 v118, v118, v149, v122
	s_cselect_b64 vcc, -1, 0
	v_dot2_u32_u16 v118, v119, v154, v118
	v_dot2_u32_u16 v119, v114, s5, 0
	v_dot2_u32_u16 v118, v120, v156, v118
	v_dot2_u32_u16 v119, v115, s5, v119
	v_dot2_u32_u16 v118, v121, v157, v118
	v_dot2_u32_u16 v119, v116, s5, v119
	s_cmp_gt_i32 s4, 7
	v_dot2_u32_u16 v119, v117, s5, v119
	v_cndmask_b32_e32 v118, v122, v118, vcc
	s_cselect_b64 vcc, -1, 0
	s_cmp_eq_u32 s4, 7
	v_add3_u32 v120, v123, v128, v119
	v_cndmask_b32_e32 v119, 0, v119, vcc
	v_add_u32_e32 v118, v119, v118
	v_dot2_u32_u16 v114, v114, v149, v118
	s_cselect_b64 vcc, -1, 0
	v_dot2_u32_u16 v114, v115, v154, v114
	v_dot2_u32_u16 v115, v110, s5, 0
	v_dot2_u32_u16 v114, v116, v156, v114
	v_dot2_u32_u16 v115, v111, s5, v115
	v_dot2_u32_u16 v114, v117, v157, v114
	v_dot2_u32_u16 v115, v112, s5, v115
	s_cmp_gt_i32 s4, 8
	v_dot2_u32_u16 v115, v113, s5, v115
	v_cndmask_b32_e32 v114, v118, v114, vcc
	s_cselect_b64 vcc, -1, 0
	s_cmp_eq_u32 s4, 8
	v_cndmask_b32_e32 v116, 0, v115, vcc
	v_add_u32_e32 v114, v116, v114
	v_dot2_u32_u16 v110, v110, v149, v114
	s_cselect_b64 vcc, -1, 0
	v_dot2_u32_u16 v110, v111, v154, v110
	v_dot2_u32_u16 v111, v106, s5, 0
	v_dot2_u32_u16 v110, v112, v156, v110
	v_dot2_u32_u16 v111, v107, s5, v111
	v_dot2_u32_u16 v110, v113, v157, v110
	v_dot2_u32_u16 v111, v108, s5, v111
	s_cmp_gt_i32 s4, 9
	v_dot2_u32_u16 v111, v109, s5, v111
	v_cndmask_b32_e32 v110, v114, v110, vcc
	s_cselect_b64 vcc, -1, 0
	s_cmp_eq_u32 s4, 9
	v_add3_u32 v112, v115, v120, v111
	v_cndmask_b32_e32 v111, 0, v111, vcc
	v_add_u32_e32 v110, v111, v110
	v_dot2_u32_u16 v106, v106, v149, v110
	s_cselect_b64 vcc, -1, 0
	v_dot2_u32_u16 v106, v107, v154, v106
	v_dot2_u32_u16 v107, v102, s5, 0
	v_dot2_u32_u16 v106, v108, v156, v106
	v_dot2_u32_u16 v107, v103, s5, v107
	v_dot2_u32_u16 v106, v109, v157, v106
	v_dot2_u32_u16 v107, v104, s5, v107
	s_cmp_gt_i32 s4, 10
	v_dot2_u32_u16 v107, v105, s5, v107
	v_cndmask_b32_e32 v106, v110, v106, vcc
	s_cselect_b64 vcc, -1, 0
	s_cmp_eq_u32 s4, 10
	v_cndmask_b32_e32 v108, 0, v107, vcc
	v_add_u32_e32 v106, v108, v106
	v_dot2_u32_u16 v102, v102, v149, v106
	s_cselect_b64 vcc, -1, 0
	v_dot2_u32_u16 v102, v103, v154, v102
	v_dot2_u32_u16 v103, v98, s5, 0
	v_dot2_u32_u16 v102, v104, v156, v102
	v_dot2_u32_u16 v103, v99, s5, v103
	v_dot2_u32_u16 v102, v105, v157, v102
	v_dot2_u32_u16 v103, v100, s5, v103
	s_cmp_gt_i32 s4, 11
	v_dot2_u32_u16 v103, v101, s5, v103
	v_cndmask_b32_e32 v102, v106, v102, vcc
	s_cselect_b64 vcc, -1, 0
	s_cmp_eq_u32 s4, 11
	v_add3_u32 v104, v107, v112, v103
	v_cndmask_b32_e32 v103, 0, v103, vcc
	v_add_u32_e32 v102, v103, v102
	v_dot2_u32_u16 v98, v98, v149, v102
	s_cselect_b64 vcc, -1, 0
	v_dot2_u32_u16 v98, v99, v154, v98
	v_dot2_u32_u16 v99, v94, s5, 0
	v_dot2_u32_u16 v98, v100, v156, v98
	v_dot2_u32_u16 v99, v95, s5, v99
	v_dot2_u32_u16 v98, v101, v157, v98
	v_dot2_u32_u16 v99, v96, s5, v99
	s_cmp_gt_i32 s4, 12
	v_dot2_u32_u16 v99, v97, s5, v99
	v_cndmask_b32_e32 v98, v102, v98, vcc
	s_cselect_b64 vcc, -1, 0
	s_cmp_eq_u32 s4, 12
	v_cndmask_b32_e32 v100, 0, v99, vcc
	v_add_u32_e32 v98, v100, v98
	v_dot2_u32_u16 v94, v94, v149, v98
	s_cselect_b64 vcc, -1, 0
	v_dot2_u32_u16 v94, v95, v154, v94
	v_dot2_u32_u16 v95, v90, s5, 0
	v_dot2_u32_u16 v94, v96, v156, v94
	v_dot2_u32_u16 v95, v91, s5, v95
	v_dot2_u32_u16 v94, v97, v157, v94
	v_dot2_u32_u16 v95, v92, s5, v95
	s_cmp_gt_i32 s4, 13
	v_dot2_u32_u16 v95, v93, s5, v95
	v_cndmask_b32_e32 v94, v98, v94, vcc
	s_cselect_b64 vcc, -1, 0
	s_cmp_eq_u32 s4, 13
	v_add3_u32 v96, v99, v104, v95
	v_cndmask_b32_e32 v95, 0, v95, vcc
	v_add_u32_e32 v94, v95, v94
	v_dot2_u32_u16 v90, v90, v149, v94
	s_cselect_b64 vcc, -1, 0
	v_dot2_u32_u16 v90, v91, v154, v90
	s_waitcnt vmcnt(23)
	v_dot2_u32_u16 v91, v86, s5, 0
	v_dot2_u32_u16 v90, v92, v156, v90
	v_dot2_u32_u16 v91, v87, s5, v91
	v_dot2_u32_u16 v90, v93, v157, v90
	v_dot2_u32_u16 v91, v88, s5, v91
	s_cmp_gt_i32 s4, 14
	v_dot2_u32_u16 v91, v89, s5, v91
	v_cndmask_b32_e32 v90, v94, v90, vcc
	s_cselect_b64 vcc, -1, 0
	s_cmp_eq_u32 s4, 14
	v_cndmask_b32_e32 v92, 0, v91, vcc
	v_add_u32_e32 v90, v92, v90
	v_dot2_u32_u16 v86, v86, v149, v90
	s_nop 0
	v_dot2_u32_u16 v86, v87, v154, v86
	v_dot2_u32_u16 v87, v82, s5, 0
	v_dot2_u32_u16 v86, v88, v156, v86
	v_mbcnt_hi_u32_b32 v88, -1, v148
	v_dot2_u32_u16 v87, v83, s5, v87
	v_and_b32_e32 v92, 64, v88
	v_add_u32_e32 v93, -1, v88
	v_dot2_u32_u16 v87, v84, s5, v87
	v_cmp_lt_i32_e32 vcc, v93, v92
	v_dot2_u32_u16 v87, v85, s5, v87
	v_dot2_u32_u16 v86, v89, v157, v86
	v_cndmask_b32_e32 v93, v93, v88, vcc
	v_lshlrev_b32_e32 v93, 2, v93
	v_add3_u32 v162, v91, v96, v87
	ds_bpermute_b32 v94, v93, v150
	ds_bpermute_b32 v87, v93, v162
	v_cmp_eq_u32_e32 vcc, 0, v147
	v_add_u32_e32 v91, -2, v88
	s_waitcnt lgkmcnt(1)
	v_cndmask_b32_e64 v89, v94, 0, vcc
	s_waitcnt lgkmcnt(0)
	v_cndmask_b32_e64 v87, v87, 0, vcc
	v_cmp_lt_i32_e32 vcc, v91, v92
	v_add_u32_e32 v89, v89, v150
	v_add_u32_e32 v87, v87, v162
	v_cndmask_b32_e32 v91, v91, v88, vcc
	v_lshlrev_b32_e32 v91, 2, v91
	ds_bpermute_b32 v93, v91, v89
	ds_bpermute_b32 v91, v91, v87
	s_cselect_b64 vcc, -1, 0
	v_cndmask_b32_e32 v86, v90, v86, vcc
	v_cmp_gt_u32_e32 vcc, 2, v147
	v_dot2_u32_u16 v82, v82, v149, v86
	s_cmp_eq_u32 s4, 15
	s_waitcnt lgkmcnt(1)
	v_cndmask_b32_e64 v90, v93, 0, vcc
	v_add_u32_e32 v89, v90, v89
	s_waitcnt lgkmcnt(0)
	v_cndmask_b32_e64 v90, v91, 0, vcc
	v_add_u32_e32 v91, -4, v88
	v_cmp_lt_i32_e32 vcc, v91, v92
	v_add_u32_e32 v87, v90, v87
	v_dot2_u32_u16 v82, v83, v154, v82
	v_cndmask_b32_e32 v91, v91, v88, vcc
	v_lshlrev_b32_e32 v91, 2, v91
	ds_bpermute_b32 v93, v91, v89
	ds_bpermute_b32 v90, v91, v87
	v_cmp_gt_u32_e32 vcc, 4, v147
	v_dot2_u32_u16 v82, v84, v156, v82
	v_cmp_eq_u32_e64 s[4:5], 63, v147
	s_waitcnt lgkmcnt(1)
	v_cndmask_b32_e64 v91, v93, 0, vcc
	v_add_u32_e32 v89, v91, v89
	v_add_u32_e32 v91, -8, v88
	s_waitcnt lgkmcnt(0)
	v_cndmask_b32_e64 v90, v90, 0, vcc
	v_cmp_lt_i32_e32 vcc, v91, v92
	v_add_u32_e32 v87, v90, v87
	v_dot2_u32_u16 v82, v85, v157, v82
	v_cndmask_b32_e32 v91, v91, v88, vcc
	v_lshlrev_b32_e32 v91, 2, v91
	ds_bpermute_b32 v93, v91, v89
	ds_bpermute_b32 v90, v91, v87
	v_cmp_gt_u32_e32 vcc, 8, v147
	s_waitcnt lgkmcnt(1)
	s_nop 0
	v_cndmask_b32_e64 v83, v93, 0, vcc
	v_add_u32_e32 v83, v83, v89
	s_waitcnt lgkmcnt(0)
	v_cndmask_b32_e64 v89, v90, 0, vcc
	v_add_u32_e32 v90, -16, v88
	v_cmp_lt_i32_e32 vcc, v90, v92
	v_add_u32_e32 v87, v89, v87
	s_nop 0
	v_cndmask_b32_e32 v90, v90, v88, vcc
	v_lshlrev_b32_e32 v90, 2, v90
	ds_bpermute_b32 v91, v90, v83
	ds_bpermute_b32 v89, v90, v87
	v_cmp_gt_u32_e32 vcc, 16, v147
	s_waitcnt lgkmcnt(1)
	s_nop 0
	v_cndmask_b32_e64 v84, v91, 0, vcc
	v_add_u32_e32 v83, v84, v83
	s_waitcnt lgkmcnt(0)
	v_cndmask_b32_e64 v84, v89, 0, vcc
	v_subrev_u32_e32 v89, 32, v88
	v_cmp_lt_i32_e32 vcc, v89, v92
	v_add_u32_e32 v84, v84, v87
	s_nop 0
	v_cndmask_b32_e32 v88, v89, v88, vcc
	v_lshlrev_b32_e32 v88, 2, v88
	ds_bpermute_b32 v89, v88, v83
	ds_bpermute_b32 v87, v88, v84
	v_cmp_gt_u32_e32 vcc, 32, v147
	s_waitcnt lgkmcnt(1)
	s_nop 0
	v_cndmask_b32_e64 v85, v89, 0, vcc
	v_add_u32_e32 v163, v85, v83
	s_waitcnt lgkmcnt(0)
	v_cndmask_b32_e64 v83, v87, 0, vcc
	v_add_u32_e32 v149, v83, v84
	s_cselect_b64 vcc, -1, 0
	s_and_saveexec_b64 s[10:11], s[4:5]
	s_cbranch_execz .LBB1_5
	v_lshlrev_b32_e32 v83, 2, v1
	v_or_b32_e32 v84, 0x23380, v83
	v_add_u32_e32 v83, 0x23390, v83
	ds_write_b32 v84, v149
	ds_write_b32 v83, v163

.LBB1_6:
	s_or_b64 exec, exec, s[6:7]
	s_ashr_i32 s15, s12, 8
	s_addk_i32 s12, 0xc35
	v_and_b32_e32 v83, 31, v0
	s_load_dwordx2 s[26:27], s[0:1], 0x68
	s_load_dwordx2 s[28:29], s[0:1], 0x30
	s_ashr_i32 s33, s12, 8
	v_lshlrev_b32_e32 v82, 3, v83
	s_movk_i32 s37, 0x110
	s_sub_i32 s34, s33, s15
	v_mad_u32_u24 v144, v155, s37, v82
	s_waitcnt vmcnt(22)
	v_cvt_pk_f16_f32 v85, v4, v5
	v_cvt_pk_f16_f32 v84, v2, v3
	s_add_i32 s4, s34, 3
	ds_write_b64 v144, v[84:85]
	s_waitcnt vmcnt(21)
	v_cvt_pk_f16_f32 v85, v8, v9
	v_cvt_pk_f16_f32 v84, v6, v7
	s_and_b32 s5, s2, 7
	ds_write_b64 v144, v[84:85] offset:4352
	s_waitcnt vmcnt(20)
	v_cvt_pk_f16_f32 v85, v76, v77
	v_cvt_pk_f16_f32 v84, v74, v75
	s_ashr_i32 s35, s4, 2
	ds_write_b64 v144, v[84:85] offset:8704
	s_waitcnt vmcnt(19)
	v_cvt_pk_f16_f32 v85, v80, v81
	v_cvt_pk_f16_f32 v84, v78, v79
	v_bfe_u32 v143, v0, 4, 2
	v_cmp_eq_u32_e64 s[12:13], s5, v1
	s_cmp_lt_i32 s35, 1
	v_lshlrev_b32_e32 v142, 2, v0
	ds_write_b64 v144, v[84:85] offset:13056
	s_waitcnt lgkmcnt(0)
	s_barrier
	s_cbranch_scc1 .LBB1_58
	s_load_dwordx2 s[10:11], s[0:1], 0x60
	s_load_dwordx8 s[16:23], s[0:1], 0x38
	s_load_dwordx4 s[4:7], s[0:1], 0x18
	s_load_dwordx2 s[30:31], s[0:1], 0x28
	s_movk_i32 s0, 0x17f
	v_mov_b32_e32 v85, 0x3f800008
	v_cmp_lt_u32_e32 vcc, s0, v0
	s_movk_i32 s0, 0x13f
	s_addk_i32 s2, 0x7f
	v_cndmask_b32_e32 v82, 0, v85, vcc
	v_cmp_lt_u32_e32 vcc, s0, v0
	s_mul_i32 s0, s3, 0x186a
	s_ashr_i32 s1, s0, 31
	s_lshl_b64 s[0:1], s[0:1], 2
	s_cmpk_lt_u32 s2, 0xff
	s_waitcnt lgkmcnt(0)
	s_cselect_b32 s18, s18, s22
	v_cndmask_b32_e32 v85, 0, v85, vcc
	s_cselect_b32 s2, s19, s23
	s_cselect_b32 s19, s17, s21
	s_cselect_b32 s20, s16, s20
	s_add_u32 s16, s18, s0
	s_waitcnt vmcnt(1)
	v_mul_f32_e32 v86, v85, v151
	s_waitcnt vmcnt(0)
	v_mul_f32_e32 v90, v85, v152
	s_addc_u32 s17, s2, s1
	v_min_u32_e32 v85, 0x69, v0
	v_mov_b32_e32 v87, 0x6000
	v_lshl_or_b32 v85, v85, 2, v87
	s_add_u32 s0, s20, s0
	s_addc_u32 s1, s19, s1
	global_load_dword v115, v85, s[16:17] nt
	global_load_dword v94, v85, s[0:1] nt
	v_or_b32_e32 v85, 0x5800, v142
	global_load_dword v95, v85, s[16:17] nt
	global_load_dword v96, v85, s[0:1] nt
	v_or_b32_e32 v85, 0x5000, v142
	global_load_dword v97, v85, s[16:17] nt
	global_load_dword v98, v85, s[0:1] nt
	v_or_b32_e32 v85, 0x4800, v142
	global_load_dword v99, v85, s[16:17] nt
	global_load_dword v100, v85, s[0:1] nt
	v_or_b32_e32 v85, 0x4000, v142
	global_load_dword v101, v85, s[16:17] nt
	global_load_dword v102, v85, s[0:1] nt
	v_or_b32_e32 v85, 0x3800, v142
	global_load_dword v103, v85, s[16:17] nt
	global_load_dword v104, v85, s[0:1] nt
	v_or_b32_e32 v85, 0x3000, v142
	v_or_b32_e32 v87, 0xa00, v0
	global_load_dword v105, v85, s[16:17] nt
	global_load_dword v106, v85, s[0:1] nt
	v_lshlrev_b32_e32 v85, 2, v87
	global_load_dword v107, v85, s[16:17] nt
	global_load_dword v108, v85, s[0:1] nt
	v_or_b32_e32 v85, 0x2000, v142
	global_load_dword v109, v85, s[16:17] nt
	global_load_dword v110, v85, s[0:1] nt
	global_load_dword v112, v142, s[0:1] nt
	v_or_b32_e32 v88, 0x600, v0
	v_lshlrev_b32_e32 v85, 2, v88
	global_load_dword v111, v85, s[16:17] nt
	global_load_dword v114, v85, s[0:1] nt
	v_or_b32_e32 v85, 0x1000, v142
	global_load_dword v117, v85, s[16:17] nt
	global_load_dword v116, v85, s[0:1] nt
	global_load_dword v119, v142, s[16:17] offset:2048 nt
	global_load_dword v118, v142, s[0:1] offset:2048 nt
	global_load_dword v122, v142, s[16:17] nt
	v_lshlrev_b32_e32 v84, 3, v0
	s_add_u32 s0, s4, 0xc35000
	v_lshlrev_b32_e32 v126, 4, v83
	v_mov_b32_e32 v127, 0
	s_movk_i32 s2, 0x200
	s_addc_u32 s1, s5, 0
	v_lshl_add_u64 v[128:129], s[24:25], 0, v[126:127]
	v_and_b32_e32 v83, 0x78, v84
	v_lshlrev_b32_e32 v126, 2, v142
	v_or_b32_e32 v85, 0x200, v0
	v_lshl_add_u64 v[130:131], s[30:31], 0, v[126:127]
	v_add_u32_e32 v152, 0x15400, v126
	v_lshlrev_b32_e32 v126, 1, v83
	v_and_b32_e32 v228, 0x10, v126
	v_and_b32_e32 v229, 0x60, v126
	v_lshrrev_b32_e32 v229, 1, v229
	v_lshl_add_u32 v229, v228, 2, v229
	v_lshrrev_b32_e32 v228, 7, v126
	v_mul_u32_u24_e32 v228, 0x61a800, v228
	v_add_u32_e32 v228, v228, v229
	v_mov_b32_e32 v229, 0
	v_mov_b32_e32 v83, s1
	v_mov_b32_e32 v84, s5
	v_cmp_gt_u32_e32 vcc, s2, v0
	v_lshrrev_b32_e32 v157, 4, v85
	v_bfe_u32 v159, v88, 4, 6
	v_cndmask_b32_e32 v85, v83, v84, vcc
	v_mov_b32_e32 v83, s0
	v_mov_b32_e32 v84, s4
	v_cndmask_b32_e32 v84, v83, v84, vcc
	v_lshl_add_u64 v[136:137], s[0:1], 0, v[228:229]
	v_mul_u32_u24_e32 v83, 0x330, v159
	s_movk_i32 s0, 0x100
	v_bfe_u32 v161, v87, 4, 6
	v_lshrrev_b32_e32 v145, 4, v0
	s_movk_i32 s16, 0x330
	v_add3_u32 v160, v83, v126, s0
	v_mul_u32_u24_e32 v83, 0x330, v161
	s_mul_i32 s0, s14, 0x101
	v_mad_u32_u24 v156, v145, s16, v126
	v_lshl_add_u64 v[132:133], s[4:5], 0, v[228:229]
	v_mad_u32_u24 v158, v157, s16, v126
	v_lshl_add_u64 v[134:135], v[84:85], 0, v[228:229]
	v_lshl_add_u64 v[138:139], s[6:7], 0, v[228:229]
	v_add3_u32 v126, v83, v126, s2
	s_cmp_eq_u32 s3, 0
	v_add_u32_e32 v120, s0, v0
	s_mov_b32 s2, 0x5397829d
	s_cselect_b64 s[16:17], -1, 0
	v_ashrrev_i32_e32 v121, 31, v120
	s_ashr_i32 s1, s0, 31
	v_lshl_add_u64 v[140:141], v[120:121], 2, s[10:11]
	s_lshl_b64 s[0:1], s[0:1], 2
	s_add_u32 s18, s10, s0
	s_movk_i32 s3, 0xff3c
	s_addc_u32 s19, s11, s1
	s_mov_b32 s20, 0xff9e
	v_mul_i32_i24_e32 v123, 0xfffffef2, v146
	v_mul_u32_u24_e32 v125, 0x60, v1
	v_mul_f32_e32 v82, v82, v153
	s_movk_i32 s38, 0xff
	v_lshlrev_b32_e32 v124, 4, v143
	s_mov_b32 s36, 0
	v_or_b32_e32 v150, 64, v155
	v_lshrrev_b32_e32 v151, 2, v0
	v_or_b32_e32 v153, 0x50, v155
	v_or_b32_e32 v154, 0x60, v155
	v_or_b32_e32 v155, 0x70, v155
	v_mov_b32_e32 v83, v82
	v_mov_b32_e32 v84, v82
	v_mov_b32_e32 v85, v82
	v_mov_b32_e32 v87, v86
	v_mov_b32_e32 v88, v86
	v_mov_b32_e32 v89, v86
	v_mov_b32_e32 v91, v90
	v_mov_b32_e32 v92, v90
	v_mov_b32_e32 v93, v90
	v_cmp_lt_u32_e64 s[4:5], 63, v0
	v_sub_u32_e32 v162, v149, v162
	v_sub_u32_e32 v163, v163, v164
	v_add_u32_e32 v164, 0x22b80, v142
	s_waitcnt vmcnt(7)
	v_mul_hi_i32 v113, v112, s2
	v_lshrrev_b32_e32 v120, 31, v113
	v_ashrrev_i32_e32 v113, 6, v113
	v_add_u32_e32 v120, v113, v120
	v_mad_u64_u32 v[112:113], s[0:1], v120, s3, v[112:113]
	v_mul_hi_i32 v113, v112, s2
	v_lshrrev_b32_e32 v121, 31, v113
	v_ashrrev_i32_e32 v113, 5, v113
	v_add_u32_e32 v113, v113, v121
	v_lshlrev_b32_e32 v121, 23, v113
	v_mul_lo_u32 v113, v113, s20
	v_add_lshl_u32 v112, v113, v112, 16
	s_waitcnt vmcnt(0)
	v_or3_b32 v168, v121, v122, v112
	v_mul_hi_i32 v112, v118, s2
	v_lshlrev_b32_e32 v120, 2, v120
	v_lshrrev_b32_e32 v113, 31, v112
	v_ashrrev_i32_e32 v112, 6, v112
	v_add_u32_e32 v167, 0x22780, v120
	v_add_u32_e32 v169, 0x22b80, v120
	v_add_u32_e32 v170, 0x22f80, v120
	v_add_u32_e32 v120, v112, v113
	v_mad_u64_u32 v[112:113], s[0:1], v120, s3, v[118:119]
	v_mul_hi_i32 v113, v112, s2
	v_lshrrev_b32_e32 v118, 31, v113
	v_ashrrev_i32_e32 v113, 5, v113
	v_add_u32_e32 v113, v113, v118
	v_lshlrev_b32_e32 v118, 2, v120
	v_lshlrev_b32_e32 v120, 23, v113
	v_mul_lo_u32 v113, v113, s20
	v_add_lshl_u32 v112, v113, v112, 16
	v_or3_b32 v172, v120, v119, v112
	v_mul_hi_i32 v112, v116, s2
	v_lshrrev_b32_e32 v113, 31, v112
	v_ashrrev_i32_e32 v112, 6, v112
	v_add_u32_e32 v171, 0x22780, v118
	v_add_u32_e32 v173, 0x22b80, v118
	v_add_u32_e32 v174, 0x22f80, v118
	v_add_u32_e32 v118, v112, v113
	v_mad_u64_u32 v[112:113], s[0:1], v118, s3, v[116:117]
	v_mul_hi_i32 v113, v112, s2
	v_lshrrev_b32_e32 v116, 31, v113
	v_ashrrev_i32_e32 v113, 5, v113
	v_add_u32_e32 v113, v113, v116
	v_lshlrev_b32_e32 v116, 2, v118
	v_lshlrev_b32_e32 v118, 23, v113
	v_mul_lo_u32 v113, v113, s20
	v_add_lshl_u32 v112, v113, v112, 16
	v_or3_b32 v176, v118, v117, v112
	v_mul_hi_i32 v112, v114, s2
	v_lshrrev_b32_e32 v113, 31, v112
	v_ashrrev_i32_e32 v112, 6, v112
	v_add_u32_e32 v175, 0x22780, v116
	v_add_u32_e32 v177, 0x22b80, v116
	v_add_u32_e32 v178, 0x22f80, v116
	v_add_u32_e32 v116, v112, v113
	v_mad_u64_u32 v[112:113], s[0:1], v116, s3, v[114:115]
	v_mul_hi_i32 v113, v112, s2
	v_lshrrev_b32_e32 v114, 31, v113
	v_ashrrev_i32_e32 v113, 5, v113
	v_add_u32_e32 v113, v113, v114
	v_lshlrev_b32_e32 v114, 2, v116
	v_lshlrev_b32_e32 v116, 23, v113
	v_mul_lo_u32 v113, v113, s20
	v_add_lshl_u32 v112, v113, v112, 16
	v_or3_b32 v180, v116, v111, v112
	v_mul_hi_i32 v111, v110, s2
	v_lshrrev_b32_e32 v112, 31, v111
	v_ashrrev_i32_e32 v111, 6, v111
	v_add_u32_e32 v112, v111, v112
	v_mad_u64_u32 v[110:111], s[0:1], v112, s3, v[110:111]
	v_mul_hi_i32 v111, v110, s2
	v_lshrrev_b32_e32 v113, 31, v111
	v_ashrrev_i32_e32 v111, 5, v111
	v_add_u32_e32 v111, v111, v113
	v_lshlrev_b32_e32 v113, 23, v111
	v_mul_lo_u32 v111, v111, s20
	v_add_lshl_u32 v110, v111, v110, 16
	v_or3_b32 v184, v113, v109, v110
	v_mul_hi_i32 v109, v108, s2
	v_lshrrev_b32_e32 v110, 31, v109
	v_ashrrev_i32_e32 v109, 6, v109
	v_add_u32_e32 v110, v109, v110
	v_mad_u64_u32 v[108:109], s[0:1], v110, s3, v[108:109]
	v_mul_hi_i32 v109, v108, s2
	v_lshrrev_b32_e32 v111, 31, v109
	v_ashrrev_i32_e32 v109, 5, v109
	v_add_u32_e32 v109, v109, v111
	v_lshlrev_b32_e32 v111, 23, v109
	v_mul_lo_u32 v109, v109, s20
	v_add_lshl_u32 v108, v109, v108, 16
	v_or3_b32 v188, v111, v107, v108
	v_mul_hi_i32 v107, v106, s2
	v_lshrrev_b32_e32 v108, 31, v107
	v_ashrrev_i32_e32 v107, 6, v107
	v_add_u32_e32 v108, v107, v108
	v_mad_u64_u32 v[106:107], s[0:1], v108, s3, v[106:107]
	v_mul_hi_i32 v107, v106, s2
	v_lshrrev_b32_e32 v109, 31, v107
	v_ashrrev_i32_e32 v107, 5, v107
	v_add_u32_e32 v107, v107, v109
	v_lshlrev_b32_e32 v109, 23, v107
	v_mul_lo_u32 v107, v107, s20
	v_add_lshl_u32 v106, v107, v106, 16
	v_or3_b32 v192, v109, v105, v106
	v_mul_hi_i32 v105, v104, s2
	v_lshrrev_b32_e32 v106, 31, v105
	v_ashrrev_i32_e32 v105, 6, v105
	v_add_u32_e32 v106, v105, v106
	v_mad_u64_u32 v[104:105], s[0:1], v106, s3, v[104:105]
	v_mul_hi_i32 v105, v104, s2
	v_lshrrev_b32_e32 v107, 31, v105
	v_ashrrev_i32_e32 v105, 5, v105
	v_add_u32_e32 v105, v105, v107
	v_lshlrev_b32_e32 v107, 23, v105
	v_mul_lo_u32 v105, v105, s20
	v_add_lshl_u32 v104, v105, v104, 16
	v_or3_b32 v196, v107, v103, v104
	v_mul_hi_i32 v103, v102, s2
	v_lshrrev_b32_e32 v104, 31, v103
	v_ashrrev_i32_e32 v103, 6, v103
	v_add_u32_e32 v104, v103, v104
	v_mad_u64_u32 v[102:103], s[0:1], v104, s3, v[102:103]
	v_mul_hi_i32 v103, v102, s2
	v_lshrrev_b32_e32 v105, 31, v103
	v_ashrrev_i32_e32 v103, 5, v103
	v_add_u32_e32 v103, v103, v105
	v_lshlrev_b32_e32 v105, 23, v103
	v_mul_lo_u32 v103, v103, s20
	v_add_lshl_u32 v102, v103, v102, 16
	v_or3_b32 v200, v105, v101, v102
	v_mul_hi_i32 v101, v100, s2
	v_lshrrev_b32_e32 v102, 31, v101
	v_ashrrev_i32_e32 v101, 6, v101
	v_add_u32_e32 v102, v101, v102
	v_mad_u64_u32 v[100:101], s[0:1], v102, s3, v[100:101]
	v_mul_hi_i32 v101, v100, s2
	v_lshrrev_b32_e32 v103, 31, v101
	v_ashrrev_i32_e32 v101, 5, v101
	v_add_u32_e32 v101, v101, v103
	v_lshlrev_b32_e32 v103, 23, v101
	v_mul_lo_u32 v101, v101, s20
	v_add_lshl_u32 v100, v101, v100, 16
	v_or3_b32 v204, v103, v99, v100
	v_mul_hi_i32 v99, v98, s2
	v_lshrrev_b32_e32 v100, 31, v99
	v_ashrrev_i32_e32 v99, 6, v99
	v_add_u32_e32 v100, v99, v100
	v_mad_u64_u32 v[98:99], s[0:1], v100, s3, v[98:99]
	v_mul_hi_i32 v99, v98, s2
	v_lshrrev_b32_e32 v101, 31, v99
	v_ashrrev_i32_e32 v99, 5, v99
	v_add_u32_e32 v99, v99, v101
	v_lshlrev_b32_e32 v101, 23, v99
	v_mul_lo_u32 v99, v99, s20
	v_add_lshl_u32 v98, v99, v98, 16
	v_or3_b32 v208, v101, v97, v98
	v_mul_hi_i32 v97, v96, s2
	v_lshrrev_b32_e32 v98, 31, v97
	v_ashrrev_i32_e32 v97, 6, v97
	v_add_u32_e32 v98, v97, v98
	v_mad_u64_u32 v[96:97], s[10:11], v98, s3, v[96:97]
	v_mul_hi_i32 v97, v96, s2
	v_lshrrev_b32_e32 v99, 31, v97
	v_ashrrev_i32_e32 v97, 5, v97
	v_add_u32_e32 v97, v97, v99
	v_lshlrev_b32_e32 v99, 23, v97
	v_mul_lo_u32 v97, v97, s20
	v_add_lshl_u32 v96, v97, v96, 16
	v_or3_b32 v212, v99, v95, v96
	v_mul_hi_i32 v95, v94, s2
	v_lshrrev_b32_e32 v96, 31, v95
	v_ashrrev_i32_e32 v95, 6, v95
	v_add_u32_e32 v96, v95, v96
	v_mad_u64_u32 v[94:95], s[22:23], v96, s3, v[94:95]
	v_mul_hi_i32 v95, v94, s2
	v_lshrrev_b32_e32 v97, 31, v95
	v_ashrrev_i32_e32 v95, 5, v95
	v_add_u32_e32 v95, v95, v97
	v_lshlrev_b32_e32 v97, 23, v95
	v_mul_lo_u32 v95, v95, s20
	v_add_lshl_u32 v94, v95, v94, 16
	v_or3_b32 v217, v97, v115, v94
	v_lshlrev_b32_e32 v94, 2, v146
	v_lshl_or_b32 v220, v143, 8, v94
	v_mul_u32_u24_e32 v94, 0xcc0, v143
	v_lshlrev_b32_e32 v112, 2, v112
	v_lshlrev_b32_e32 v110, 2, v110
	v_lshlrev_b32_e32 v108, 2, v108
	v_lshlrev_b32_e32 v106, 2, v106
	v_lshlrev_b32_e32 v104, 2, v104
	v_lshlrev_b32_e32 v102, 2, v102
	v_lshlrev_b32_e32 v100, 2, v100
	s_movk_i32 s0, 0x26a
	v_lshlrev_b32_e32 v98, 2, v98
	s_movk_i32 s10, 0x6a
	v_lshlrev_b32_e32 v96, 2, v96
	v_add3_u32 v94, v123, v125, v94
	v_mul_u32_u24_e32 v95, 0x110, v146
	s_mov_b32 s2, 0x8800
	v_add_u32_e32 v165, 0x22f80, v142
	v_add_u32_e32 v166, 0x22780, v142
	v_cmp_eq_u32_e64 s[6:7], s38, v0
	v_add_u32_e32 v179, 0x22780, v114
	v_add_u32_e32 v181, 0x22b80, v114
	v_add_u32_e32 v182, 0x22f80, v114
	v_add_u32_e32 v183, 0x22780, v112
	v_add_u32_e32 v185, 0x22b80, v112
	v_add_u32_e32 v186, 0x22f80, v112
	v_add_u32_e32 v187, 0x22780, v110
	v_add_u32_e32 v189, 0x22b80, v110
	v_add_u32_e32 v190, 0x22f80, v110
	v_add_u32_e32 v191, 0x22780, v108
	v_add_u32_e32 v193, 0x22b80, v108
	v_add_u32_e32 v194, 0x22f80, v108
	v_add_u32_e32 v195, 0x22780, v106
	v_add_u32_e32 v197, 0x22b80, v106
	v_add_u32_e32 v198, 0x22f80, v106
	v_add_u32_e32 v199, 0x22780, v104
	v_add_u32_e32 v201, 0x22b80, v104
	v_add_u32_e32 v202, 0x22f80, v104
	v_add_u32_e32 v203, 0x22780, v102
	v_add_u32_e32 v205, 0x22b80, v102
	v_add_u32_e32 v206, 0x22f80, v102
	v_add_u32_e32 v207, 0x22780, v100
	v_add_u32_e32 v209, 0x22b80, v100
	v_add_u32_e32 v210, 0x22f80, v100
	v_cmp_gt_u32_e64 s[0:1], s0, v0
	v_add_u32_e32 v211, 0x22780, v98
	v_add_u32_e32 v213, 0x22b80, v98
	v_add_u32_e32 v214, 0x22f80, v98
	v_cmp_gt_u32_e64 s[10:11], s10, v0
	v_add_u32_e32 v216, 0x22780, v96
	v_add_u32_e32 v218, 0x22b80, v96
	v_add_u32_e32 v219, 0x22f80, v96
	v_add3_u32 v221, v94, v95, s2
	v_mad_u32_u24 v222, v146, s37, v124
	v_mov_b32_e32 v215, 0xff800000
	s_mov_b64 s[20:21], 0
	s_movk_i32 s37, 0x4400
	v_mov_b32_e32 v223, 1
.LBB1_8:
	s_lshl_b32 s2, s36, 2
	s_add_i32 s24, s2, s15
	s_add_i32 s38, s36, 1
	s_cmp_lt_i32 s38, s35
	s_cselect_b64 s[22:23], -1, 0
	s_cmp_ge_i32 s38, s35
	s_cbranch_scc1 .LBB1_10
	s_lshl_b32 s2, s24, 4
	s_waitcnt vmcnt(3)
	v_add_u32_e32 v2, s2, v150
	v_add_u32_e32 v4, s2, v153
	s_waitcnt vmcnt(1)
	v_add_u32_e32 v74, s2, v154
	v_add_u32_e32 v76, s2, v155
	v_min_i32_e32 v2, 0xc34f, v2
	v_min_i32_e32 v4, 0xc34f, v4
	v_min_i32_e32 v74, 0xc34f, v74
	v_min_i32_e32 v76, 0xc34f, v76
	v_ashrrev_i32_e32 v3, 31, v2
	v_ashrrev_i32_e32 v5, 31, v4
	v_ashrrev_i32_e32 v75, 31, v74
	v_ashrrev_i32_e32 v77, 31, v76
	v_lshlrev_b64 v[2:3], 9, v[2:3]
	v_lshlrev_b64 v[4:5], 9, v[4:5]
	v_lshlrev_b64 v[74:75], 9, v[74:75]
	v_lshlrev_b64 v[76:77], 9, v[76:77]
	v_lshl_add_u64 v[2:3], v[128:129], 0, v[2:3]
	v_lshl_add_u64 v[6:7], v[128:129], 0, v[4:5]
	v_lshl_add_u64 v[74:75], v[128:129], 0, v[74:75]
	s_waitcnt vmcnt(0)
	v_lshl_add_u64 v[78:79], v[128:129], 0, v[76:77]
	global_load_dwordx4 v[2:5], v[2:3], off nt
	s_nop 0
	global_load_dwordx4 v[6:9], v[6:7], off nt
	s_nop 0
	global_load_dwordx4 v[74:77], v[74:75], off nt
	s_nop 0
	global_load_dwordx4 v[78:81], v[78:79], off nt

_Z10agg_kernelPKjPKiPKDF16_S4_PKfS4_S0_S2_S2_S2_S2_Pf:
	s_and_b32 s3, s2, 1
	s_lshr_b32 s4, s2, 1
	s_load_dwordx16 s[8:23], s[0:1], 0x0
	s_load_dwordx8 s[24:31], s[0:1], 0x40
	s_mul_i32 s6, s4, 0xc4
	s_sub_u32 s5, 0xc350, s6
	s_min_u32 s5, s5, 0xc4
	v_lshrrev_b32_e32 v2, 2, v0
	v_and_b32_e32 v1, 3, v0
	v_lshrrev_b32_e32 v13, 1, v1
	v_lshl_add_u32 v13, s3, 1, v13
	v_lshlrev_b32_e32 v13, 2, v13
	v_lshlrev_b32_e32 v1, 4, v1
	s_lshl_b32 s52, s4, 2
	s_waitcnt lgkmcnt(0)
	s_add_u32 s52, s10, s52
	s_addc_u32 s53, s11, 0
	s_load_dwordx2 s[32:33], s[52:53], 0x0
	s_load_dwordx2 s[36:37], s[52:53], 0x404
	v_add_u32_e32 v40, s6, v2
	v_min_u32_e32 v40, 0xc34f, v40
	v_lshlrev_b32_e32 v40, 6, v40
	v_add3_u32 v40, v40, v13, 16
	global_load_dword v3, v40, s[16:17]
	global_load_dword v4, v40, s[16:17] offset:32
	v_lshlrev_b32_e32 v62, 2, v0
	v_mov_b32_e32 v63, 0
	ds_write_b32 v62, v63 offset:21248
	v_cmp_gt_u32_e32 vcc, 0x200, v0
	s_and_saveexec_b64 s[60:61], vcc
	ds_write_b32 v62, v63 offset:25344
	s_mov_b64 exec, s[60:61]
	s_waitcnt lgkmcnt(0)
	s_sub_u32 s38, s33, s32
	s_sub_u32 s39, s37, s36
	s_lshl_b32 s52, s32, 2
	s_add_u32 s42, s8, s52
	s_addc_u32 s43, s9, 0
	s_add_u32 s52, s36, 0xc3500
	s_lshl_b32 s52, s52, 2
	s_add_u32 s44, s8, s52
	s_addc_u32 s45, s9, 0
	s_max_i32 s52, s38, 1
	s_sub_u32 s52, s52, 1
	s_max_i32 s53, s39, 1
	s_sub_u32 s53, s53, 1
	s_movk_i32 s46, 0x80
	s_movk_i32 s55, 0x62
	s_movk_i32 s47, 0x61a8
	v_min_u32_e32 v41, s52, v0
	v_lshlrev_b32_e32 v41, 2, v41
	global_load_dword v8, v41, s[42:43] nt
	v_min_u32_e32 v41, s53, v0
	v_lshlrev_b32_e32 v41, 2, v41
	global_load_dword v24, v41, s[44:45] nt
	v_add_u32_e32 v40, 0x400, v0
	v_min_u32_e32 v41, s52, v40
	v_lshlrev_b32_e32 v41, 2, v41
	global_load_dword v9, v41, s[42:43] nt
	v_min_u32_e32 v41, s53, v40
	v_lshlrev_b32_e32 v41, 2, v41
	global_load_dword v25, v41, s[44:45] nt
	v_add_u32_e32 v40, 0x800, v0
	v_min_u32_e32 v41, s52, v40
	v_lshlrev_b32_e32 v41, 2, v41
	global_load_dword v10, v41, s[42:43] nt
	v_min_u32_e32 v41, s53, v40
	v_lshlrev_b32_e32 v41, 2, v41
	global_load_dword v26, v41, s[44:45] nt
	v_add_u32_e32 v40, 0xc00, v0
	v_min_u32_e32 v41, s52, v40
	v_lshlrev_b32_e32 v41, 2, v41
	global_load_dword v11, v41, s[42:43] nt
	v_min_u32_e32 v41, s53, v40
	v_lshlrev_b32_e32 v41, 2, v41
	global_load_dword v27, v41, s[44:45] nt
	v_mov_b32_e32 v61, 1
	v_mov_b32_e32 v43, 0xc4
	s_barrier
	s_waitcnt vmcnt(7)
	v_bfe_u32 v28, v8, 16, 7
	v_bfe_u32 v42, v8, 23, 1
	v_and_b32_e32 v44, 0xffff, v8
	v_mad_u32_u24 v28, v42, s55, v28
	v_cmp_le_u32_e32 vcc, s47, v44
	v_lshlrev_b32_e32 v28, 2, v28
	s_nop 0
	v_cndmask_b32_e32 v42, 0, v43, vcc
	v_lshl_add_u32 v28, v42, 2, v28
	v_cmp_gt_u32_e32 vcc, s38, v0
	s_and_saveexec_b64 s[60:61], vcc
	ds_add_rtn_u32 v16, v28, v61 offset:21248
	s_mov_b64 exec, s[60:61]
	s_waitcnt vmcnt(6)
	v_bfe_u32 v32, v24, 16, 7
	v_bfe_u32 v42, v24, 23, 1
	v_and_b32_e32 v44, 0xffff, v24
	v_mad_u32_u24 v32, v42, s55, v32
	v_cmp_le_u32_e32 vcc, s47, v44
	v_lshlrev_b32_e32 v32, 2, v32
	s_nop 0
	v_cndmask_b32_e32 v42, 0, v43, vcc
	v_lshl_add_u32 v32, v42, 2, v32
	v_cmp_gt_u32_e32 vcc, s39, v0
	s_and_saveexec_b64 s[60:61], vcc
	ds_add_rtn_u32 v20, v32, v61 offset:23296
	s_mov_b64 exec, s[60:61]
	s_waitcnt vmcnt(5)
	v_add_u32_e32 v40, 0x400, v0
	v_bfe_u32 v29, v9, 16, 7
	v_bfe_u32 v42, v9, 23, 1
	v_and_b32_e32 v44, 0xffff, v9
	v_mad_u32_u24 v29, v42, s55, v29
	v_cmp_le_u32_e32 vcc, s47, v44
	v_lshlrev_b32_e32 v29, 2, v29
	s_nop 0
	v_cndmask_b32_e32 v42, 0, v43, vcc
	v_lshl_add_u32 v29, v42, 2, v29
	v_cmp_gt_u32_e32 vcc, s38, v40
	s_and_saveexec_b64 s[60:61], vcc
	ds_add_rtn_u32 v17, v29, v61 offset:21248
	s_mov_b64 exec, s[60:61]
	s_waitcnt vmcnt(4)
	v_bfe_u32 v33, v25, 16, 7
	v_bfe_u32 v42, v25, 23, 1
	v_and_b32_e32 v44, 0xffff, v25
	v_mad_u32_u24 v33, v42, s55, v33
	v_cmp_le_u32_e32 vcc, s47, v44
	v_lshlrev_b32_e32 v33, 2, v33
	s_nop 0
	v_cndmask_b32_e32 v42, 0, v43, vcc
	v_lshl_add_u32 v33, v42, 2, v33
	v_cmp_gt_u32_e32 vcc, s39, v40
	s_and_saveexec_b64 s[60:61], vcc
	ds_add_rtn_u32 v21, v33, v61 offset:23296
	s_mov_b64 exec, s[60:61]
	s_waitcnt vmcnt(3)
	v_add_u32_e32 v40, 0x800, v0
	v_bfe_u32 v30, v10, 16, 7
	v_bfe_u32 v42, v10, 23, 1
	v_and_b32_e32 v44, 0xffff, v10
	v_mad_u32_u24 v30, v42, s55, v30
	v_cmp_le_u32_e32 vcc, s47, v44
	v_lshlrev_b32_e32 v30, 2, v30
	s_nop 0
	v_cndmask_b32_e32 v42, 0, v43, vcc
	v_lshl_add_u32 v30, v42, 2, v30
	v_cmp_gt_u32_e32 vcc, s38, v40
	s_and_saveexec_b64 s[60:61], vcc
	ds_add_rtn_u32 v18, v30, v61 offset:21248
	s_mov_b64 exec, s[60:61]
	s_waitcnt vmcnt(2)
	v_bfe_u32 v34, v26, 16, 7
	v_bfe_u32 v42, v26, 23, 1
	v_and_b32_e32 v44, 0xffff, v26
	v_mad_u32_u24 v34, v42, s55, v34
	v_cmp_le_u32_e32 vcc, s47, v44
	v_lshlrev_b32_e32 v34, 2, v34
	s_nop 0
	v_cndmask_b32_e32 v42, 0, v43, vcc
	v_lshl_add_u32 v34, v42, 2, v34
	v_cmp_gt_u32_e32 vcc, s39, v40
	s_and_saveexec_b64 s[60:61], vcc
	ds_add_rtn_u32 v22, v34, v61 offset:23296
	s_mov_b64 exec, s[60:61]
	s_waitcnt vmcnt(1)
	v_add_u32_e32 v40, 0xc00, v0
	v_bfe_u32 v31, v11, 16, 7
	v_bfe_u32 v42, v11, 23, 1
	v_and_b32_e32 v44, 0xffff, v11
	v_mad_u32_u24 v31, v42, s55, v31
	v_cmp_le_u32_e32 vcc, s47, v44
	v_lshlrev_b32_e32 v31, 2, v31
	s_nop 0
	v_cndmask_b32_e32 v42, 0, v43, vcc
	v_lshl_add_u32 v31, v42, 2, v31
	v_cmp_gt_u32_e32 vcc, s38, v40
	s_and_saveexec_b64 s[60:61], vcc
	ds_add_rtn_u32 v19, v31, v61 offset:21248
	s_mov_b64 exec, s[60:61]
	s_waitcnt vmcnt(0)
	v_bfe_u32 v35, v27, 16, 7
	v_bfe_u32 v42, v27, 23, 1
	v_and_b32_e32 v44, 0xffff, v27
	v_mad_u32_u24 v35, v42, s55, v35
	v_cmp_le_u32_e32 vcc, s47, v44
	v_lshlrev_b32_e32 v35, 2, v35
	s_nop 0
	v_cndmask_b32_e32 v42, 0, v43, vcc
	v_lshl_add_u32 v35, v42, 2, v35
	v_cmp_gt_u32_e32 vcc, s39, v40
	s_and_saveexec_b64 s[60:61], vcc
	ds_add_rtn_u32 v23, v35, v61 offset:23296
	s_mov_b64 exec, s[60:61]
	s_waitcnt lgkmcnt(0)
	s_barrier
	ds_read_b32 v40, v62 offset:21248
	v_and_b32_e32 v44, 63, v0
	v_lshrrev_b32_e32 v45, 6, v0
	v_lshlrev_b32_e32 v45, 2, v45
	v_and_b32_e32 v52, 0x1ff, v0
	v_lshrrev_b32_e32 v51, 9, v0
	v_cmp_le_u32_e32 vcc, 0xc4, v52
	v_mov_b32_e32 v47, 31
	s_nop 0
	v_cndmask_b32_e64 v53, 0, 1, vcc
	v_mul_u32_u24_e32 v54, 0xc4, v53
	v_sub_u32_e32 v54, v52, v54
	v_lshl_add_u32 v53, v51, 1, v53
	s_waitcnt lgkmcnt(0)
	v_min_u32_e32 v55, 31, v40
	v_sub_u32_e32 v55, v47, v55
	v_and_b32_e32 v47, 3, v0
	v_lshl_or_b32 v55, v55, 2, v47
	v_lshl_add_u32 v55, v53, 7, v55
	v_lshlrev_b32_e32 v55, 2, v55
	v_cmp_gt_u32_e32 vcc, 0x188, v52
	s_and_saveexec_b64 s[60:61], vcc
	ds_add_rtn_u32 v51, v55, v61 offset:25344
	s_mov_b64 exec, s[60:61]
	v_mov_b32_e32 v41, v40
	s_nop 1
	v_add_u32_dpp v41, v41, v41 row_shr:1 row_mask:0xf bank_mask:0xf
	s_nop 1
	v_add_u32_dpp v41, v41, v41 row_shr:2 row_mask:0xf bank_mask:0xf
	s_nop 1
	v_add_u32_dpp v41, v41, v41 row_shr:4 row_mask:0xf bank_mask:0xf
	s_nop 1
	v_add_u32_dpp v41, v41, v41 row_shr:8 row_mask:0xf bank_mask:0xf
	s_nop 1
	v_add_u32_dpp v41, v41, v41 row_bcast:15 row_mask:0xa bank_mask:0xf
	s_nop 1
	v_add_u32_dpp v41, v41, v41 row_bcast:31 row_mask:0xc bank_mask:0xf
	v_cmp_eq_u32_e32 vcc, 63, v44
	s_and_saveexec_b64 s[60:61], vcc
	ds_write_b32 v45, v41 offset:21056
	s_mov_b64 exec, s[60:61]
	s_waitcnt lgkmcnt(0)
	s_barrier
	v_cmp_gt_u32_e32 vcc, 0x200, v0
	s_and_saveexec_b64 s[60:61], vcc
	s_cbranch_execz .Lagg_bins_done
	ds_read_b32 v48, v62 offset:25344
	s_waitcnt lgkmcnt(0)
	v_mov_b32_e32 v49, v48
	s_nop 1
	v_add_u32_dpp v49, v49, v49 row_shr:1 row_mask:0xf bank_mask:0xf
	s_nop 1
	v_add_u32_dpp v49, v49, v49 row_shr:2 row_mask:0xf bank_mask:0xf
	s_nop 1
	v_add_u32_dpp v49, v49, v49 row_shr:4 row_mask:0xf bank_mask:0xf
	s_nop 1
	v_add_u32_dpp v49, v49, v49 row_shr:8 row_mask:0xf bank_mask:0xf
	s_nop 1
	v_add_u32_dpp v49, v49, v49 row_bcast:15 row_mask:0xa bank_mask:0xf
	s_nop 1
	v_add_u32_dpp v49, v49, v49 row_bcast:31 row_mask:0xc bank_mask:0xf
	s_nop 0
	v_sub_u32_e32 v50, v49, v48
	ds_write_b32 v62, v50 offset:29440
	v_cmp_eq_u32_e32 vcc, 63, v44
	s_and_b64 exec, exec, vcc
	ds_write_b32 v45, v49 offset:33536
